# v049 + retention scan: the masked-out (dummy) att fragment loads run with EXEC = lane 0 only (one line instead of eight)
# speedup vs baseline: 1.0129x; 1.0090x over previous
; #define LAS __attribute__((address_space(3)))
; __device__ __forceinline__ unsigned cvt_pk_bf16(float lo, float hi) { const f32x2 v = {lo, hi}; const bf16v2_t r = __builtin_convertvector(v, bf16v2_t); return __builtin_bit_cast(unsigned, r); }
; __device__ __forceinline__ void ph_rscan(const int vc, const Params& p, LAS unsigned char* lds) {
;     ...
;         for (int ks = 0; ks < 8; ++ks) {
;             S = __builtin_amdgcn_mfma_f32_32x32x16_bf16(kf[ks], vs[ks], S, 0, 0, 0);
;             if (ks < 4 && att_need(ks)) {
; #pragma unroll
;                 for (int nt = 0; nt < 2; ++nt) oa[nt] = __builtin_amdgcn_mfma_f32_16x16x32_bf16(bv[2 * ks + nt], af[ks], oa[nt], 0, 0, 0); }
;         }
;         __builtin_amdgcn_sched_barrier(0);
;         { const bf16_t* apn = ATT + (size_t)cn * 16384 + (size_t)w * 4 * 512 + l * 8;
; #pragma unroll
;           for (int ks = 0; ks < 4; ++ks) { const int kse = att_need(ks) ? ks : (dir ? 3 : 0);
;               af[ks] = *(const bf16x8*)(apn + kse * 512); }
;           const bf16_t* kp = KT + (((size_t)h * 132 + (tbn >> 7)) * 8 + w) * 8 * 512 + l * 8;
; #pragma unroll
;           for (int ks = 0; ks < 8; ++ks) kf[ks] = *(const bf16x8*)(kp + ks * 512); }
;         {
;             bf16_t* obase = si < 2 ? dump : Ob + (size_t)tokbase(si) * 2048;
;             const int t = 16 * w + (l & 15); const float qs = qd[t];
;             bf16_t* orow = obase + (size_t)t * 2048 + h * 512 + sl * 32 + 4 * (l >> 4);
; #pragma unroll
;             for (int nt = 0; nt < 2; ++nt) { const f32x4 o = oi[nt] * qs + oa[nt]; u32x2 wv; wv.x = cvt_pk_bf16(o[0], o[1]); wv.y = cvt_pk_bf16(o[2], o[3]); *(u32x2*)(orow + 16 * nt) = wv; }
;         }
; #pragma unroll
;         for (int g = 0; g < 4; ++g) { u32x2 wv; wv.x = cvt_pk_bf16(S[4 * g], S[4 * g + 1]); wv.y = cvt_pk_bf16(S[4 * g + 2], S[4 * g + 3]);
;             *(LAS u32x2*)(STl + ((cur ^ 1) * 32 + (l & 31)) * RS_ST + 32 * w + 8 * g + 4 * (l >> 5)) = wv; }
;         stage_v(vnext, cur ^ 1);
.LBB0_1784:
	s_waitcnt vmcnt(14) lgkmcnt(3)
	v_mfma_f32_32x32x16_bf16 v[2:17], v[34:37], v[126:129], v[2:17]
	s_waitcnt vmcnt(13) lgkmcnt(2)
	v_mfma_f32_32x32x16_bf16 v[2:17], v[30:33], v[122:125], v[2:17]
	s_waitcnt vmcnt(12) lgkmcnt(1)
	v_mfma_f32_32x32x16_bf16 v[2:17], v[26:29], v[114:117], v[2:17]
	s_waitcnt vmcnt(11) lgkmcnt(0)
	v_mfma_f32_32x32x16_bf16 v[2:17], v[18:21], v[110:113], v[2:17]
	s_ashr_i32 s43, s42, 31
	s_lshl_b64 s[8:9], s[42:43], 15
	v_lshl_add_u64 v[18:19], v[194:195], 0, s[8:9]
	v_lshl_add_u64 v[20:21], v[18:19], 0, s[2:3]
	s_ashr_i32 s2, s40, 7
	s_ashr_i32 s9, s2, 31
	s_add_u32 s8, s2, s50
	s_mov_b32 s27, s3
	s_mov_b32 s29, s3
	s_mov_b32 s31, s3
	s_addc_u32 s9, s9, 0
	v_lshl_add_u64 v[22:23], v[18:19], 0, s[26:27]
	s_or_b64 exec, s[6:7], 1
	global_load_dwordx4 v[94:97], v[20:21], off
	s_or_b64 exec, s[20:21], 1
	global_load_dwordx4 v[90:93], v[22:23], off
	s_mov_b64 exec, -1
	v_lshl_add_u64 v[20:21], v[18:19], 0, s[28:29]
	v_lshl_add_u64 v[18:19], v[18:19], 0, s[30:31]
	s_lshl_b64 s[8:9], s[8:9], 16
	s_or_b64 exec, s[22:23], 1
	global_load_dwordx4 v[82:85], v[20:21], off
	s_or_b64 exec, s[24:25], 1
	global_load_dwordx4 v[78:81], v[18:19], off
	s_mov_b64 exec, -1
	v_lshl_add_u64 v[18:19], v[196:197], 0, s[8:9]
	v_add_co_u32_e32 v30, vcc, s51, v18
	global_load_dwordx4 v[86:89], v[18:19], off
	global_load_dwordx4 v[74:77], v[18:19], off offset:1024
	global_load_dwordx4 v[38:41], v[18:19], off offset:2048
	global_load_dwordx4 v[34:37], v[18:19], off offset:3072
	v_addc_co_u32_e32 v31, vcc, 0, v19, vcc
	global_load_dwordx4 v[18:21], v[30:31], off
	global_load_dwordx4 v[26:29], v[30:31], off offset:1024
	global_load_dwordx4 v[22:25], v[30:31], off offset:2048
	s_nop 0
	global_load_dwordx4 v[30:33], v[30:31], off offset:3072
	s_lshl_b32 s2, s59, 7
	s_add_i32 s8, s2, s55
	s_ashr_i32 s9, s8, 31
	s_lshl_b64 s[8:9], s[8:9], 12
	s_add_u32 s2, s47, s8
	ds_read_b32 v110, v205
	s_addc_u32 s10, s48, s9
	s_and_b64 s[8:9], s[38:39], exec
	s_cselect_b32 s9, s19, s10
	s_cselect_b32 s8, s18, s2
	v_lshl_add_u64 v[112:113], s[8:9], 0, v[200:201]
	s_mov_b32 s35, s3
	v_lshl_add_u64 v[112:113], v[112:113], 0, s[34:35]
	s_mov_b32 s37, s3
	s_waitcnt lgkmcnt(0)
	v_pk_fma_f32 v[100:101], v[100:101], v[110:111], v[104:105] op_sel_hi:[1,0,1]
	v_pk_fma_f32 v[98:99], v[98:99], v[110:111], v[102:103] op_sel_hi:[1,0,1]
	v_lshl_add_u64 v[112:113], v[112:113], 0, s[36:37]
	v_pk_fma_f32 v[108:109], v[108:109], v[110:111], v[120:121] op_sel_hi:[1,0,1]
	v_pk_fma_f32 v[106:107], v[106:107], v[110:111], v[118:119] op_sel_hi:[1,0,1]
	v_cvt_pk_bf16_f32 v102, v98, v99
	v_cvt_pk_bf16_f32 v103, v100, v101
	v_cvt_pk_bf16_f32 v98, v2, v3
	v_cvt_pk_bf16_f32 v99, v4, v5
	v_cvt_pk_bf16_f32 v100, v6, v7
	v_cvt_pk_bf16_f32 v101, v8, v9
	v_lshl_add_u64 v[112:113], v[112:113], 0, v[186:187]
	v_cvt_pk_bf16_f32 v106, v106, v107
	v_cvt_pk_bf16_f32 v107, v108, v109
	ds_write2_b64 v206, v[98:99], v[100:101] offset1:2
	v_cvt_pk_bf16_f32 v98, v10, v11
	v_cvt_pk_bf16_f32 v99, v12, v13
	v_cvt_pk_bf16_f32 v100, v14, v15
	v_cvt_pk_bf16_f32 v101, v16, v17
	global_store_dwordx2 v[112:113], v[106:107], off
	ds_write2_b64 v206, v[98:99], v[100:101] offset0:4 offset1:6
	s_waitcnt vmcnt(21)
	ds_write_b128 v1, v[130:133] offset:33792
	ds_read_b128 v[98:101], v199
	global_store_dwordx2 v[112:113], v[102:103], off offset:32
	ds_read_b128 v[102:105], v199 offset:16
	v_lshlrev_b32_e32 v106, 16, v130
	v_and_b32_e32 v107, 0xffff0000, v130
	s_waitcnt lgkmcnt(1)
	v_pk_mul_f32 v[98:99], v[98:99], v[106:107]
	v_lshlrev_b32_e32 v106, 16, v131
	v_and_b32_e32 v107, 0xffff0000, v131
	v_pk_mul_f32 v[100:101], v[100:101], v[106:107]
	v_cvt_pk_bf16_f32 v98, v98, v99
	v_cvt_pk_bf16_f32 v99, v100, v101
	v_lshlrev_b32_e32 v100, 16, v132
	v_and_b32_e32 v101, 0xffff0000, v132
	s_waitcnt lgkmcnt(0)
	v_pk_mul_f32 v[100:101], v[102:103], v[100:101]
	v_lshlrev_b32_e32 v102, 16, v133
	v_and_b32_e32 v103, 0xffff0000, v133
	v_pk_mul_f32 v[102:103], v[104:105], v[102:103]
	s_add_i32 s2, s58, 2
	s_add_i32 s49, s49, 2
	s_add_i32 s57, s57, -2
	v_cvt_pk_bf16_f32 v100, v100, v101
	v_cvt_pk_bf16_f32 v101, v102, v103
	s_cmp_gt_u32 s58, 63
	s_mov_b32 s58, s2
	ds_write_b128 v1, v[98:101] offset:51200
	s_cbranch_scc1 .LBB0_1807

; __device__ __forceinline__ void ph_rscan(const int vc, const Params& p, LAS unsigned char* lds) {
;     ...
;         for (int ks = 0; ks < 8; ++ks) {
;             S = __builtin_amdgcn_mfma_f32_32x32x16_bf16(kf[ks], vs[ks], S, 0, 0, 0);
;             if (ks < 4 && att_need(ks)) {
; #pragma unroll
;                 for (int nt = 0; nt < 2; ++nt) oa[nt] = __builtin_amdgcn_mfma_f32_16x16x32_bf16(bv[2 * ks + nt], af[ks], oa[nt], 0, 0, 0); }
;         }
;         __builtin_amdgcn_sched_barrier(0);
;         { const bf16_t* apn = ATT + (size_t)cn * 16384 + (size_t)w * 4 * 512 + l * 8;
; #pragma unroll
;           for (int ks = 0; ks < 4; ++ks) { const int kse = att_need(ks) ? ks : (dir ? 3 : 0);
;               af[ks] = *(const bf16x8*)(apn + kse * 512); }
;           const bf16_t* kp = KT + (((size_t)h * 132 + (tbn >> 7)) * 8 + w) * 8 * 512 + l * 8;
; #pragma unroll
;           for (int ks = 0; ks < 8; ++ks) kf[ks] = *(const bf16x8*)(kp + ks * 512); }
;         {
;             bf16_t* obase = si < 2 ? dump : Ob + (size_t)tokbase(si) * 2048;
.LBB0_1797:
	s_waitcnt vmcnt(14) lgkmcnt(3)
	v_mfma_f32_32x32x16_bf16 v[2:17], v[18:21], v[62:65], v[2:17]
	s_waitcnt vmcnt(13) lgkmcnt(2)
	v_mfma_f32_32x32x16_bf16 v[2:17], v[26:29], v[58:61], v[2:17]
	s_waitcnt vmcnt(12) lgkmcnt(1)
	v_mfma_f32_32x32x16_bf16 v[2:17], v[22:25], v[54:57], v[2:17]
	s_waitcnt vmcnt(11) lgkmcnt(0)
	v_mfma_f32_32x32x16_bf16 v[2:17], v[30:33], v[50:53], v[2:17]
	s_ashr_i32 s45, s44, 31
	s_lshl_b64 s[44:45], s[44:45], 15
	v_lshl_add_u64 v[18:19], v[194:195], 0, s[44:45]
	s_lshl_b32 s2, s54, 1
	s_mov_b32 s27, s3
	v_lshl_add_u64 v[20:21], v[18:19], 0, s[2:3]
	v_lshl_add_u64 v[22:23], v[18:19], 0, s[26:27]
	s_mov_b32 s29, s3
	s_ashr_i32 s27, s42, 7
	s_or_b64 exec, s[6:7], 1
	global_load_dwordx4 v[90:93], v[20:21], off
	s_or_b64 exec, s[20:21], 1
	global_load_dwordx4 v[82:85], v[22:23], off
	s_mov_b64 exec, -1
	v_lshl_add_u64 v[20:21], v[18:19], 0, s[28:29]
	s_ashr_i32 s29, s27, 31
	s_add_u32 s42, s27, s50
	s_mov_b32 s31, s3
	s_addc_u32 s43, s29, 0
	v_lshl_add_u64 v[18:19], v[18:19], 0, s[30:31]
	s_lshl_b64 s[42:43], s[42:43], 16
	s_or_b64 exec, s[22:23], 1
	global_load_dwordx4 v[74:77], v[20:21], off
	s_or_b64 exec, s[24:25], 1
	global_load_dwordx4 v[22:25], v[18:19], off
	s_mov_b64 exec, -1
	v_lshl_add_u64 v[18:19], v[196:197], 0, s[42:43]
	global_load_dwordx4 v[94:97], v[18:19], off
	global_load_dwordx4 v[86:89], v[18:19], off offset:1024
	global_load_dwordx4 v[78:81], v[18:19], off offset:2048
	global_load_dwordx4 v[38:41], v[18:19], off offset:3072
	v_add_co_u32_e32 v18, vcc, 0x1000, v18
	s_nop 1
	v_addc_co_u32_e32 v19, vcc, 0, v19, vcc
	global_load_dwordx4 v[34:37], v[18:19], off
	global_load_dwordx4 v[30:33], v[18:19], off offset:1024
	global_load_dwordx4 v[26:29], v[18:19], off offset:2048
	s_nop 0
	global_load_dwordx4 v[18:21], v[18:19], off offset:3072
	s_andn2_b64 vcc, exec, s[40:41]
	s_mov_b64 s[40:41], s[18:19]
	s_cbranch_vccnz .LBB0_1799
	s_add_i32 s27, s49, -3
	s_add_i32 s29, s57, 1
	s_and_b64 s[40:41], s[0:1], exec
	s_cselect_b32 s27, s27, s29
	s_lshl_b32 s27, s27, 7
	s_add_i32 s40, s27, s55
	s_ashr_i32 s41, s40, 31
	s_lshl_b64 s[40:41], s[40:41], 12
	s_add_u32 s40, s47, s40
	s_addc_u32 s41, s48, s41
